# first-unit gathered-row index loads of the gate/up GEMM also batched
# speedup vs baseline: 1.0092x; 1.0027x over previous
; DEVI int opaque_tid() { int t = threadIdx.x; asm volatile("" : "+v"(t)); return t; }
; #define PG8_STAGEB(bufoff, gbase) PG8_STAGE2(bufoff, gbase, voffB[0], voffB[1])
; #define PG8_BAR __builtin_amdgcn_s_barrier()
; template <class Sched, class Epi, bool FP8 = false>
; DEVI void gemm_phase(LAS unsigned char* lds, const int K, const Sched& S, const Epi& E) {
;     const int tid = opaque_tid(), wid = __builtin_amdgcn_readfirstlane(tid >> 6), lane = tid & 63, wr = wid >> 2, wc = wid & 3, fr = lane & 15, fq = lane >> 4;
;     const int nt = K / BK;
;     int R0, C0, R1, C1; stage_rc(tid * 16, R0, C0); stage_rc(tid * 16 + 8192, R1, C1);
;     unsigned voffB[2];
;     { const int Rb0 = Epi::PERM ? ((R0 & ~31) + perm32(R0 & 31)) : R0, Rb1 = Epi::PERM ? ((R1 & ~31) + perm32(R1 & 31)) : R1;
;       voffB[0] = (unsigned)(Rb0 * K + C0) * 2u; voffB[1] = (unsigned)(Rb1 * K + C1) * 2u; }
;     const size_t kstep = (size_t)(BK * 2);
;     const size_t hstepB = (size_t)HALF * K * 2;
;     const unsigned ldsw = (unsigned)wid * 1024u;
;     const int aoff = lds_byte(wr * 64 + fr, fq * 8), boff = lds_byte(wc * 32 + fr, fq * 8);
;     ...
;     Unit cur, nxt; int ui = 0;
;     if (!S.next(0, cur)) return;
;     f32x4 acc[2][2][4][2];
; #pragma unroll
;     for (int a = 0; a < 2; ++a)
; #pragma unroll
;         for (int b = 0; b < 2; ++b)
; #pragma unroll
;             for (int m = 0; m < 4; ++m)
; #pragma unroll
;                 for (int n = 0; n < 2; ++n) acc[a][b][m][n] = (f32x4){0.f, 0.f, 0.f, 0.f};
;     bf16x8 At[4][2], B0[2][2], B1[2][2];
;     i32x8 At8[4], B08[2], B18[2];
;     const int mx_one = 0x7f7f7f7f;
;     unsigned vc[4], vn[4];
;     S.aoff(cur, R0, C0, R1, C1, vc);
;     const char* cA = cur.A; const char* cB = cur.B;
;     PG8_STAGEB(PG8_SB(0, 0), cB); PG8_STAGEB(PG8_SB(0, 1), cB + hstepB); PG8_STAGE2(PG8_SA(0, 0), cA, vc[0], vc[1]); PG8_STAGE2(PG8_SA(0, 1), cA, vc[2], vc[3]);
;     if (wr == 1) PG8_BAR;
;     PG8_WAIT_V(2); PG8_BAR;
;     DEVI unsigned one(const pg8::Unit& u, int R, int C) const { const int slot = u.pm * 256 + R; const int row = (slot < mvalid) ? selrow[u.e * MSLOT + slot] : 0; return (unsigned)(row * (DM / 2) + C) * 2u; }
;     DEVI void aoff(const pg8::Unit& u, int R0, int C0, int R1, int C1, unsigned (&o)[4]) const { o[0] = one(u, R0, C0); o[1] = one(u, R1, C1); o[2] = one(u, 128 + R0, C0); o[3] = one(u, 128 + R1, C1); }
.LBB0_1237:
	s_andn2_b64 vcc, exec, s[28:29]
	s_cbranch_vccnz .LBB0_1295
	s_waitcnt vmcnt(0)
	v_ashrrev_i32_e32 v4, 31, v1
	v_lshrrev_b32_e32 v4, 26, v4
	v_add_u32_e32 v4, v1, v4
	v_ashrrev_i32_e32 v5, 6, v4
	v_bfe_i32 v4, v1, 27, 1
	v_lshlrev_b32_e32 v9, 4, v1
	v_lshrrev_b32_e32 v4, 22, v4
	v_add_u32_e32 v4, v9, v4
	v_and_b32_e32 v4, 0xfffffc00, v4
	v_sub_u32_e32 v4, v9, v4
	v_lshrrev_b32_e32 v6, 4, v4
	v_bitop3_b32 v6, v6, v4, 32 bitop3:0x6c
	v_ashrrev_i32_e32 v4, 31, v4
	v_readlane_b32 s6, v254, 49
	v_lshrrev_b32_e32 v4, 26, v4
	v_readlane_b32 s7, v254, 50
	v_lshlrev_b32_e32 v7, 3, v5
	v_add_u32_e32 v4, v6, v4
	s_and_b64 s[6:7], s[6:7], exec
	s_movk_i32 s5, 0x480
	v_and_b32_e32 v7, -16, v7
	v_ashrrev_i32_e32 v4, 6, v4
	s_cselect_b32 s47, s5, 0x400
	v_add_u32_e32 v197, v4, v7
	s_lshl_b32 s5, s73, 8
	v_add_u32_e32 v10, s5, v197
	v_cmp_gt_i32_e32 vcc, s47, v10
	v_mov_b32_e32 v8, 0
	v_mov_b32_e32 v7, 0
	s_and_saveexec_b64 s[28:29], vcc
	s_cbranch_execz .LBB0_1240
	s_mul_i32 s6, s46, 0x500
	v_add_u32_e32 v10, s6, v10
	v_readlane_b32 s6, v254, 24
	v_ashrrev_i32_e32 v11, 31, v10
	v_readlane_b32 s7, v254, 25
	s_nop 1
	v_lshl_add_u64 v[10:11], v[10:11], 2, s[6:7]
	global_load_dword v7, v[10:11], off
.LBB0_1240:
	s_or_b64 exec, exec, s[28:29]
	v_add_u32_e32 v9, 0x2000, v9
	v_ashrrev_i32_e32 v10, 31, v9
	v_lshrrev_b32_e32 v10, 22, v10
	v_add_u32_e32 v10, v9, v10
	v_ashrrev_i32_e32 v10, 10, v10
	v_mul_i32_i24_e32 v11, 0x400, v10
	v_sub_u32_e32 v9, v9, v11
	v_lshrrev_b32_e32 v11, 4, v9
	v_bitop3_b32 v11, v11, v9, 32 bitop3:0x6c
	v_lshlrev_b32_e32 v9, 3, v10
	v_and_b32_e32 v12, -16, v9
	v_ashrrev_i32_e32 v9, 31, v11
	v_lshrrev_b32_e32 v9, 26, v9
	v_add_u32_e32 v9, v11, v9
	v_ashrrev_i32_e32 v9, 6, v9
	v_add_u32_e32 v220, v9, v12
	v_add_u32_e32 v12, s5, v220
	v_cmp_gt_i32_e32 vcc, s47, v12
	s_and_saveexec_b64 s[28:29], vcc
	s_cbranch_execz .LBB0_1242
	s_mul_i32 s6, s46, 0x500
	v_add_u32_e32 v12, s6, v12
	v_readlane_b32 s6, v254, 24
	v_ashrrev_i32_e32 v13, 31, v12
	v_readlane_b32 s7, v254, 25
	s_nop 1
	v_lshl_add_u64 v[12:13], v[12:13], 2, s[6:7]
	global_load_dword v8, v[12:13], off
.LBB0_1242:
	s_or_b64 exec, exec, s[28:29]
	v_add_u32_e32 v221, 0x80, v197
	v_add_u32_e32 v14, s5, v221
	v_cmp_gt_i32_e32 vcc, s47, v14
	v_mov_b32_e32 v12, 0
	v_mov_b32_e32 v13, 0
	s_and_saveexec_b64 s[28:29], vcc
	s_cbranch_execz .LBB0_1244
	s_mul_i32 s6, s46, 0x500
	v_add_u32_e32 v14, s6, v14
	v_readlane_b32 s6, v254, 24
	v_ashrrev_i32_e32 v15, 31, v14
	v_readlane_b32 s7, v254, 25
	s_nop 1
	v_lshl_add_u64 v[14:15], v[14:15], 2, s[6:7]
	global_load_dword v13, v[14:15], off
.LBB0_1244:
	s_or_b64 exec, exec, s[28:29]
	v_add_u32_e32 v241, 0x80, v220
	v_add_u32_e32 v14, s5, v241
	v_cmp_gt_i32_e32 vcc, s47, v14
	s_and_saveexec_b64 s[28:29], vcc
	s_cbranch_execz .LBB0_1246
	s_mul_i32 s5, s46, 0x500
	v_add_u32_e32 v14, s5, v14
	v_readlane_b32 s6, v254, 24
	v_ashrrev_i32_e32 v15, 31, v14
	v_readlane_b32 s7, v254, 25
	s_nop 1
	v_lshl_add_u64 v[14:15], v[14:15], 2, s[6:7]
	global_load_dword v12, v[14:15], off
.LBB0_1246:
	s_or_b64 exec, exec, s[28:29]
	s_waitcnt vmcnt(0)
	v_lshlrev_b32_e32 v7, 10, v7
	v_lshlrev_b32_e32 v8, 10, v8
	v_lshlrev_b32_e32 v13, 10, v13
	v_lshlrev_b32_e32 v12, 10, v12
	v_mul_i32_i24_e32 v14, 64, v4
	v_lshlrev_b32_e32 v5, 5, v5
	v_sub_u32_e32 v6, v6, v14
	v_mov_b32_e32 v14, 1
	v_and_b32_e32 v5, 32, v5
	v_ashrrev_i16_sdwa v6, v14, sext(v6) dst_sel:DWORD dst_unused:UNUSED_PAD src0_sel:DWORD src1_sel:BYTE_0
	v_add_u32_sdwa v242, v5, sext(v6) dst_sel:DWORD dst_unused:UNUSED_PAD src0_sel:DWORD src1_sel:WORD_0
	v_lshlrev_b32_e32 v6, 6, v9
	v_lshlrev_b32_e32 v5, 5, v10
	v_sub_u32_e32 v6, v11, v6
	v_and_b32_e32 v5, 32, v5
	v_ashrrev_i16_sdwa v6, v14, sext(v6) dst_sel:DWORD dst_unused:UNUSED_PAD src0_sel:DWORD src1_sel:BYTE_0
	v_add_u32_sdwa v243, v5, sext(v6) dst_sel:DWORD dst_unused:UNUSED_PAD src0_sel:DWORD src1_sel:WORD_0
	v_lshlrev_b32_e32 v5, 1, v197
	v_lshrrev_b32_e32 v6, 2, v197
	v_and_b32_e32 v4, 3, v4
	s_mov_b32 s7, 0x1fffe0
	v_and_b32_e32 v5, 24, v5
	v_and_b32_e32 v6, 4, v6
	v_and_or_b32 v4, v197, s7, v4
	v_add_lshl_u32 v206, v7, v242, 1
	s_ashr_i32 s5, s4, 6
	v_or3_b32 v4, v4, v6, v5
	v_lshlrev_b32_e32 v5, 1, v220
	v_lshrrev_b32_e32 v6, 2, v220
	v_and_b32_e32 v7, 3, v9
	v_and_b32_e32 v5, 24, v5
	v_and_b32_e32 v6, 4, v6
	v_and_or_b32 v7, v220, s7, v7
	s_lshl_b32 s24, s5, 10
	v_or3_b32 v5, v7, v6, v5
	v_lshlrev_b32_e32 v6, 1, v242
	s_add_i32 s25, s24, 0
	v_lshl_add_u32 v198, v4, 11, v6
	s_add_i32 m0, s25, 0x10000
	s_ashr_i32 s6, s4, 8
	v_lshlrev_b32_e32 v4, 1, v243
	global_load_lds_dwordx4 v198, s[16:17]
	s_add_i32 m0, s25, 0x12000
	v_lshl_add_u32 v200, v5, 11, v4
	s_add_u32 s28, s16, 0x40000
	global_load_lds_dwordx4 v200, s[16:17]
	s_addc_u32 s29, s17, 0
	s_add_i32 m0, s25, 0x14000
	s_add_i32 s81, s25, 0x2000
	global_load_lds_dwordx4 v198, s[28:29]
	s_add_i32 m0, s25, 0x16000
	v_add_lshl_u32 v204, v8, v243, 1
	global_load_lds_dwordx4 v200, s[28:29]
	v_readlane_b32 s28, v253, 2
	s_mov_b32 m0, s25
	v_readlane_b32 s29, v253, 3
	s_add_i32 s94, s25, 0x4000
	v_add_lshl_u32 v202, v13, v242, 1
	s_add_i32 s78, s25, 0x6000
	v_add_lshl_u32 v208, v12, v243, 1
	v_mov_b32_e32 v199, v3
	global_load_lds_dwordx4 v206, s[28:29]
	s_mov_b32 m0, s81
	v_mov_b32_e32 v201, v3
	global_load_lds_dwordx4 v204, s[28:29]
	s_mov_b32 m0, s94
	v_mov_b32_e32 v207, v3
	global_load_lds_dwordx4 v202, s[28:29]
	s_mov_b32 m0, s78
	v_mov_b32_e32 v205, v3
	global_load_lds_dwordx4 v208, s[28:29]
	s_cmp_eq_u32 s6, 1
	v_lshl_add_u64 v[10:11], s[16:17], 0, v[198:199]
	v_lshl_add_u64 v[6:7], s[16:17], 0, v[200:201]
	v_lshl_add_u64 v[4:5], s[28:29], 0, v[206:207]
	s_cselect_b64 s[50:51], -1, 0
	s_cmp_lg_u32 s6, 1
	v_lshl_add_u64 v[8:9], s[28:29], 0, v[204:205]
	s_cbranch_scc1 .LBB0_1248
	s_barrier
